# in-projection K-loop only: the leading half waits for its staged pieces at the end of its compute segment
# baseline (speedup 1.0000x reference)
.LBB0_185:
	s_ashr_i32 s23, s22, 31
	s_lshl_b64 s[24:25], s[22:23], 19
	s_add_u32 s24, s19, s24
	s_addc_u32 s25, s33, s25
	s_and_b64 s[26:27], s[4:5], exec
	s_cselect_b32 s7, s25, s35
	s_cselect_b32 s9, s24, s34
	s_ashr_i32 s21, s20, 31
	s_lshl_b64 s[26:27], s[20:21], 19
	s_add_u32 s26, s38, s26
	s_addc_u32 s27, s39, s27
	s_and_b64 s[36:37], s[4:5], exec
	s_cselect_b32 s21, s27, s31
	s_cselect_b32 s23, s26, s30
	s_add_u32 s53, s30, 0x4000
	s_addc_u32 s54, s31, 0
	s_add_u32 s30, s34, 0x40080
	s_addc_u32 s31, s35, 0
	s_mov_b32 s55, -2
	ds_read_b128 v[26:29], v191
	ds_read_b128 v[30:33], v191 offset:1024
	ds_read_b128 v[18:21], v191 offset:2048
	ds_read_b128 v[22:25], v191 offset:3072
	ds_read_b128 v[10:13], v192
	ds_read_b128 v[14:17], v192 offset:1024
	ds_read_b128 v[2:5], v192 offset:2048
	ds_read_b128 v[6:9], v192 offset:3072
	s_add_u32 s0, s30, 0xfffc0080
	s_addc_u32 s1, s31, -1
	s_cmp_eq_u32 s55, 12
	s_cselect_b32 s37, s7, s1
	s_cselect_b32 s36, s9, s0
	s_cselect_b32 s35, s21, s54
	s_cselect_b32 s34, s23, s53
	v_lshl_add_u64 v[184:185], s[30:31], 0, v[176:177]
	s_add_i32 m0, s29, 0xc000
	ds_read_b128 v[196:199], v193
	ds_read_b128 v[200:203], v193 offset:1024
	ds_read_b128 v[204:207], v193 offset:2048
	ds_read_b128 v[208:211], v193 offset:3072
	ds_read_b128 v[212:215], v193 offset:4096
	ds_read_b128 v[216:219], v193 offset:5120
	ds_read_b128 v[220:223], v193 offset:6144
	ds_read_b128 v[224:227], v193 offset:7168
	global_load_lds_dwordx4 v[184:185], off
	v_lshl_add_u64 v[184:185], s[30:31], 0, v[178:179]
	s_add_i32 m0, s29, 0xe000
	s_nop 0
	global_load_lds_dwordx4 v[184:185], off
	s_and_b64 vcc, exec, s[14:15]
	s_cbranch_vccnz .Lwa_186p_0
	s_waitcnt vmcnt(8)
.Lwa_186p_0:
	s_waitcnt lgkmcnt(0)
	s_barrier
	s_setprio 1
	s_waitcnt lgkmcnt(0)
	v_mfma_scale_f32_16x16x128_f8f6f4 v[158:161], v[26:33], v[196:203], 0, v194, v194 op_sel_hi:[0,0,0]
	v_mfma_scale_f32_16x16x128_f8f6f4 v[154:157], v[18:25], v[196:203], 0, v194, v194 op_sel_hi:[0,0,0]
	v_mfma_scale_f32_16x16x128_f8f6f4 v[142:145], v[26:33], v[204:211], 0, v194, v194 op_sel_hi:[0,0,0]
	v_mfma_scale_f32_16x16x128_f8f6f4 v[138:141], v[18:25], v[204:211], 0, v194, v194 op_sel_hi:[0,0,0]
	v_mfma_scale_f32_16x16x128_f8f6f4 v[126:129], v[26:33], v[212:219], 0, v194, v194 op_sel_hi:[0,0,0]
	v_mfma_scale_f32_16x16x128_f8f6f4 v[122:125], v[18:25], v[212:219], 0, v194, v194 op_sel_hi:[0,0,0]
	v_mfma_scale_f32_16x16x128_f8f6f4 v[110:113], v[26:33], v[220:227], 0, v194, v194 op_sel_hi:[0,0,0]
	v_mfma_scale_f32_16x16x128_f8f6f4 v[106:109], v[18:25], v[220:227], 0, v194, v194 op_sel_hi:[0,0,0]
	s_setprio 0
	s_setprio 1
	v_mfma_scale_f32_16x16x128_f8f6f4 v[150:153], v[10:17], v[196:203], 0, v194, v194 op_sel_hi:[0,0,0]
	v_mfma_scale_f32_16x16x128_f8f6f4 v[146:149], v[2:9], v[196:203], 0, v194, v194 op_sel_hi:[0,0,0]
	v_mfma_scale_f32_16x16x128_f8f6f4 v[134:137], v[10:17], v[204:211], 0, v194, v194 op_sel_hi:[0,0,0]
	v_mfma_scale_f32_16x16x128_f8f6f4 v[130:133], v[2:9], v[204:211], 0, v194, v194 op_sel_hi:[0,0,0]
	v_mfma_scale_f32_16x16x128_f8f6f4 v[118:121], v[10:17], v[212:219], 0, v194, v194 op_sel_hi:[0,0,0]
	v_mfma_scale_f32_16x16x128_f8f6f4 v[114:117], v[2:9], v[212:219], 0, v194, v194 op_sel_hi:[0,0,0]
	v_mfma_scale_f32_16x16x128_f8f6f4 v[102:105], v[10:17], v[220:227], 0, v194, v194 op_sel_hi:[0,0,0]
	v_mfma_scale_f32_16x16x128_f8f6f4 v[98:101], v[2:9], v[220:227], 0, v194, v194 op_sel_hi:[0,0,0]
	s_cbranch_vccz .Lwb_186p_0
	s_waitcnt vmcnt(8)
.Lwb_186p_0:
	s_setprio 0
	s_barrier
	s_add_i32 s0, s49, s40
	v_lshl_add_u64 v[184:185], s[34:35], 0, v[164:165]
	s_mov_b32 m0, s0
	ds_read_b128 v[196:199], v193 offset:16384
	ds_read_b128 v[200:203], v193 offset:17408
	ds_read_b128 v[204:207], v193 offset:18432
	ds_read_b128 v[208:211], v193 offset:19456
	ds_read_b128 v[212:215], v193 offset:20480
	ds_read_b128 v[216:219], v193 offset:21504
	ds_read_b128 v[220:223], v193 offset:22528
	ds_read_b128 v[224:227], v193 offset:23552
	global_load_lds_dwordx4 v[184:185], off
	s_add_i32 m0, s0, 0x2000
	s_add_u32 s56, s34, 0x40000
	v_lshl_add_u64 v[184:185], s[34:35], 0, v[168:169]
	s_addc_u32 s57, s35, 0
	s_add_i32 s0, s50, s40
	global_load_lds_dwordx4 v[184:185], off
	v_lshl_add_u64 v[184:185], s[56:57], 0, v[164:165]
	s_mov_b32 m0, s0
	v_lshl_add_u64 v[186:187], s[36:37], 0, v[166:167]
	global_load_lds_dwordx4 v[184:185], off
	v_lshl_add_u64 v[184:185], s[56:57], 0, v[168:169]
	s_add_i32 m0, s0, 0x2000
	s_nop 0
	global_load_lds_dwordx4 v[184:185], off
	v_lshl_add_u64 v[184:185], s[36:37], 0, v[162:163]
	s_mov_b32 m0, s29
	s_nop 0
	global_load_lds_dwordx4 v[184:185], off
	s_mov_b32 m0, s41
	s_nop 0
	global_load_lds_dwordx4 v[186:187], off
	s_and_b64 vcc, exec, s[14:15]
	s_cbranch_vccnz .Lwa_186p_1
	s_waitcnt vmcnt(8)
.Lwa_186p_1:
	s_waitcnt lgkmcnt(0)
	s_barrier
	s_setprio 1
	s_waitcnt lgkmcnt(0)
	v_mfma_scale_f32_16x16x128_f8f6f4 v[94:97], v[26:33], v[196:203], 0, v194, v194 op_sel_hi:[0,0,0]
	v_mfma_scale_f32_16x16x128_f8f6f4 v[90:93], v[18:25], v[196:203], 0, v194, v194 op_sel_hi:[0,0,0]
	v_mfma_scale_f32_16x16x128_f8f6f4 v[78:81], v[26:33], v[204:211], 0, v194, v194 op_sel_hi:[0,0,0]
	v_mfma_scale_f32_16x16x128_f8f6f4 v[74:77], v[18:25], v[204:211], 0, v194, v194 op_sel_hi:[0,0,0]
	v_mfma_scale_f32_16x16x128_f8f6f4 v[62:65], v[26:33], v[212:219], 0, v194, v194 op_sel_hi:[0,0,0]
	v_mfma_scale_f32_16x16x128_f8f6f4 v[58:61], v[18:25], v[212:219], 0, v194, v194 op_sel_hi:[0,0,0]
	v_mfma_scale_f32_16x16x128_f8f6f4 v[46:49], v[26:33], v[220:227], 0, v194, v194 op_sel_hi:[0,0,0]
	v_mfma_scale_f32_16x16x128_f8f6f4 v[42:45], v[18:25], v[220:227], 0, v194, v194 op_sel_hi:[0,0,0]
	s_setprio 0
	s_setprio 1
	v_mfma_scale_f32_16x16x128_f8f6f4 v[86:89], v[10:17], v[196:203], 0, v194, v194 op_sel_hi:[0,0,0]
	v_mfma_scale_f32_16x16x128_f8f6f4 v[82:85], v[2:9], v[196:203], 0, v194, v194 op_sel_hi:[0,0,0]
	v_mfma_scale_f32_16x16x128_f8f6f4 v[70:73], v[10:17], v[204:211], 0, v194, v194 op_sel_hi:[0,0,0]
	v_mfma_scale_f32_16x16x128_f8f6f4 v[66:69], v[2:9], v[204:211], 0, v194, v194 op_sel_hi:[0,0,0]
	v_mfma_scale_f32_16x16x128_f8f6f4 v[54:57], v[10:17], v[212:219], 0, v194, v194 op_sel_hi:[0,0,0]
	v_mfma_scale_f32_16x16x128_f8f6f4 v[50:53], v[2:9], v[212:219], 0, v194, v194 op_sel_hi:[0,0,0]
	v_mfma_scale_f32_16x16x128_f8f6f4 v[38:41], v[10:17], v[220:227], 0, v194, v194 op_sel_hi:[0,0,0]
	v_mfma_scale_f32_16x16x128_f8f6f4 v[34:37], v[2:9], v[220:227], 0, v194, v194 op_sel_hi:[0,0,0]
	s_cbranch_vccz .Lwb_186p_1
	s_waitcnt vmcnt(8)
.Lwb_186p_1:
	s_setprio 0
	s_barrier
	s_branch .Lmid_186
.LBB0_186:
	ds_read_b128 v[26:29], v191
	ds_read_b128 v[30:33], v191 offset:1024
	ds_read_b128 v[18:21], v191 offset:2048
	ds_read_b128 v[22:25], v191 offset:3072
	ds_read_b128 v[10:13], v192
	ds_read_b128 v[14:17], v192 offset:1024
	ds_read_b128 v[2:5], v192 offset:2048
	ds_read_b128 v[6:9], v192 offset:3072
	s_add_u32 s0, s30, 0xfffc0080
	s_addc_u32 s1, s31, -1
	s_cmp_eq_u32 s55, 12
	s_cselect_b32 s37, s7, s1
	s_cselect_b32 s36, s9, s0
	s_cselect_b32 s35, s21, s54
	s_cselect_b32 s34, s23, s53
	v_lshl_add_u64 v[184:185], s[30:31], 0, v[176:177]
	s_add_i32 m0, s29, 0xc000
	ds_read_b128 v[196:199], v193
	ds_read_b128 v[200:203], v193 offset:1024
	ds_read_b128 v[204:207], v193 offset:2048
	ds_read_b128 v[208:211], v193 offset:3072
	ds_read_b128 v[212:215], v193 offset:4096
	ds_read_b128 v[216:219], v193 offset:5120
	ds_read_b128 v[220:223], v193 offset:6144
	ds_read_b128 v[224:227], v193 offset:7168
	global_load_lds_dwordx4 v[184:185], off
	v_lshl_add_u64 v[184:185], s[30:31], 0, v[178:179]
	s_add_i32 m0, s29, 0xe000
	s_nop 0
	global_load_lds_dwordx4 v[184:185], off
	s_and_b64 vcc, exec, s[14:15]
	s_cbranch_vccnz .Lwa_186l_0
	s_waitcnt vmcnt(8)
.Lwa_186l_0:
	s_waitcnt lgkmcnt(0)
	s_barrier
	s_setprio 1
	s_waitcnt lgkmcnt(0)
	v_mfma_scale_f32_16x16x128_f8f6f4 v[158:161], v[26:33], v[196:203], v[158:161], v194, v194 op_sel_hi:[0,0,0]
	v_mfma_scale_f32_16x16x128_f8f6f4 v[154:157], v[18:25], v[196:203], v[154:157], v194, v194 op_sel_hi:[0,0,0]
	v_mfma_scale_f32_16x16x128_f8f6f4 v[142:145], v[26:33], v[204:211], v[142:145], v194, v194 op_sel_hi:[0,0,0]
	v_mfma_scale_f32_16x16x128_f8f6f4 v[138:141], v[18:25], v[204:211], v[138:141], v194, v194 op_sel_hi:[0,0,0]
	v_mfma_scale_f32_16x16x128_f8f6f4 v[126:129], v[26:33], v[212:219], v[126:129], v194, v194 op_sel_hi:[0,0,0]
	v_mfma_scale_f32_16x16x128_f8f6f4 v[122:125], v[18:25], v[212:219], v[122:125], v194, v194 op_sel_hi:[0,0,0]
	v_mfma_scale_f32_16x16x128_f8f6f4 v[110:113], v[26:33], v[220:227], v[110:113], v194, v194 op_sel_hi:[0,0,0]
	v_mfma_scale_f32_16x16x128_f8f6f4 v[106:109], v[18:25], v[220:227], v[106:109], v194, v194 op_sel_hi:[0,0,0]
	s_setprio 0
	s_setprio 1
	v_mfma_scale_f32_16x16x128_f8f6f4 v[150:153], v[10:17], v[196:203], v[150:153], v194, v194 op_sel_hi:[0,0,0]
	v_mfma_scale_f32_16x16x128_f8f6f4 v[146:149], v[2:9], v[196:203], v[146:149], v194, v194 op_sel_hi:[0,0,0]
	v_mfma_scale_f32_16x16x128_f8f6f4 v[134:137], v[10:17], v[204:211], v[134:137], v194, v194 op_sel_hi:[0,0,0]
	v_mfma_scale_f32_16x16x128_f8f6f4 v[130:133], v[2:9], v[204:211], v[130:133], v194, v194 op_sel_hi:[0,0,0]
	v_mfma_scale_f32_16x16x128_f8f6f4 v[118:121], v[10:17], v[212:219], v[118:121], v194, v194 op_sel_hi:[0,0,0]
	v_mfma_scale_f32_16x16x128_f8f6f4 v[114:117], v[2:9], v[212:219], v[114:117], v194, v194 op_sel_hi:[0,0,0]
	v_mfma_scale_f32_16x16x128_f8f6f4 v[102:105], v[10:17], v[220:227], v[102:105], v194, v194 op_sel_hi:[0,0,0]
	v_mfma_scale_f32_16x16x128_f8f6f4 v[98:101], v[2:9], v[220:227], v[98:101], v194, v194 op_sel_hi:[0,0,0]
	s_cbranch_vccz .Lwb_186l_0
	s_waitcnt vmcnt(8)

.Lwa_186l_1:
	s_waitcnt lgkmcnt(0)
	s_barrier
	s_setprio 1
	s_waitcnt lgkmcnt(0)
	v_mfma_scale_f32_16x16x128_f8f6f4 v[94:97], v[26:33], v[196:203], v[94:97], v194, v194 op_sel_hi:[0,0,0]
	v_mfma_scale_f32_16x16x128_f8f6f4 v[90:93], v[18:25], v[196:203], v[90:93], v194, v194 op_sel_hi:[0,0,0]
	v_mfma_scale_f32_16x16x128_f8f6f4 v[78:81], v[26:33], v[204:211], v[78:81], v194, v194 op_sel_hi:[0,0,0]
	v_mfma_scale_f32_16x16x128_f8f6f4 v[74:77], v[18:25], v[204:211], v[74:77], v194, v194 op_sel_hi:[0,0,0]
	v_mfma_scale_f32_16x16x128_f8f6f4 v[62:65], v[26:33], v[212:219], v[62:65], v194, v194 op_sel_hi:[0,0,0]
	v_mfma_scale_f32_16x16x128_f8f6f4 v[58:61], v[18:25], v[212:219], v[58:61], v194, v194 op_sel_hi:[0,0,0]
	v_mfma_scale_f32_16x16x128_f8f6f4 v[46:49], v[26:33], v[220:227], v[46:49], v194, v194 op_sel_hi:[0,0,0]
	v_mfma_scale_f32_16x16x128_f8f6f4 v[42:45], v[18:25], v[220:227], v[42:45], v194, v194 op_sel_hi:[0,0,0]
	s_setprio 0
	s_setprio 1
	v_mfma_scale_f32_16x16x128_f8f6f4 v[86:89], v[10:17], v[196:203], v[86:89], v194, v194 op_sel_hi:[0,0,0]
	v_mfma_scale_f32_16x16x128_f8f6f4 v[82:85], v[2:9], v[196:203], v[82:85], v194, v194 op_sel_hi:[0,0,0]
	v_mfma_scale_f32_16x16x128_f8f6f4 v[70:73], v[10:17], v[204:211], v[70:73], v194, v194 op_sel_hi:[0,0,0]
	v_mfma_scale_f32_16x16x128_f8f6f4 v[66:69], v[2:9], v[204:211], v[66:69], v194, v194 op_sel_hi:[0,0,0]
	v_mfma_scale_f32_16x16x128_f8f6f4 v[54:57], v[10:17], v[212:219], v[54:57], v194, v194 op_sel_hi:[0,0,0]
	v_mfma_scale_f32_16x16x128_f8f6f4 v[50:53], v[2:9], v[212:219], v[50:53], v194, v194 op_sel_hi:[0,0,0]
	v_mfma_scale_f32_16x16x128_f8f6f4 v[38:41], v[10:17], v[220:227], v[38:41], v194, v194 op_sel_hi:[0,0,0]
	v_mfma_scale_f32_16x16x128_f8f6f4 v[34:37], v[2:9], v[220:227], v[34:37], v194, v194 op_sel_hi:[0,0,0]
	s_cbranch_vccz .Lwb_186l_1
	s_waitcnt vmcnt(8)
.Lwb_186l_1:
	s_setprio 0
	s_barrier
.Lmid_186:
	s_add_i32 s0, 0, 0x18000
	v_add_u32_e32 v0, s0, v189
	s_add_i32 s1, 0, 0x1c000
	ds_read_b128 v[2:5], v0
	ds_read_b128 v[6:9], v0 offset:1024
	ds_read_b128 v[10:13], v0 offset:2048
	ds_read_b128 v[14:17], v0 offset:3072
	v_add_u32_e32 v0, s1, v189
	ds_read_b128 v[18:21], v0
	ds_read_b128 v[22:25], v0 offset:1024
	ds_read_b128 v[26:29], v0 offset:2048
	ds_read_b128 v[30:33], v0 offset:3072
	s_add_u32 s36, s36, 0x40000
	s_addc_u32 s37, s37, 0
	s_mov_b32 m0, s42
	v_lshl_add_u64 v[228:229], s[36:37], 0, v[162:163]
	ds_read_b128 v[196:199], v193 offset:32768
	ds_read_b128 v[200:203], v193 offset:33792
	ds_read_b128 v[204:207], v193 offset:34816
	ds_read_b128 v[208:211], v193 offset:35840
	ds_read_b128 v[212:215], v193 offset:36864
	ds_read_b128 v[216:219], v193 offset:37888
	ds_read_b128 v[220:223], v193 offset:38912
	ds_read_b128 v[224:227], v193 offset:39936
	global_load_lds_dwordx4 v[228:229], off
	v_lshl_add_u64 v[228:229], s[36:37], 0, v[166:167]
	s_mov_b32 m0, s43
	s_nop 0
	global_load_lds_dwordx4 v[228:229], off
	s_and_b64 vcc, exec, s[14:15]
	s_cbranch_vccnz .Lwa_186l_2
	s_waitcnt vmcnt(8)
.Lwa_186l_2:
	s_waitcnt lgkmcnt(0)
	s_barrier
	s_setprio 1
	s_waitcnt lgkmcnt(0)
	v_mfma_scale_f32_16x16x128_f8f6f4 v[158:161], v[2:9], v[196:203], v[158:161], v194, v194 op_sel_hi:[0,0,0]
	v_mfma_scale_f32_16x16x128_f8f6f4 v[154:157], v[10:17], v[196:203], v[154:157], v194, v194 op_sel_hi:[0,0,0]
	v_mfma_scale_f32_16x16x128_f8f6f4 v[142:145], v[2:9], v[204:211], v[142:145], v194, v194 op_sel_hi:[0,0,0]
	v_mfma_scale_f32_16x16x128_f8f6f4 v[138:141], v[10:17], v[204:211], v[138:141], v194, v194 op_sel_hi:[0,0,0]
	v_mfma_scale_f32_16x16x128_f8f6f4 v[126:129], v[2:9], v[212:219], v[126:129], v194, v194 op_sel_hi:[0,0,0]
	v_mfma_scale_f32_16x16x128_f8f6f4 v[122:125], v[10:17], v[212:219], v[122:125], v194, v194 op_sel_hi:[0,0,0]
	v_mfma_scale_f32_16x16x128_f8f6f4 v[110:113], v[2:9], v[220:227], v[110:113], v194, v194 op_sel_hi:[0,0,0]
	v_mfma_scale_f32_16x16x128_f8f6f4 v[106:109], v[10:17], v[220:227], v[106:109], v194, v194 op_sel_hi:[0,0,0]
	s_setprio 0
	s_setprio 1
	v_mfma_scale_f32_16x16x128_f8f6f4 v[150:153], v[18:25], v[196:203], v[150:153], v194, v194 op_sel_hi:[0,0,0]
	v_mfma_scale_f32_16x16x128_f8f6f4 v[146:149], v[26:33], v[196:203], v[146:149], v194, v194 op_sel_hi:[0,0,0]
	v_mfma_scale_f32_16x16x128_f8f6f4 v[134:137], v[18:25], v[204:211], v[134:137], v194, v194 op_sel_hi:[0,0,0]
	v_mfma_scale_f32_16x16x128_f8f6f4 v[130:133], v[26:33], v[204:211], v[130:133], v194, v194 op_sel_hi:[0,0,0]
	v_mfma_scale_f32_16x16x128_f8f6f4 v[118:121], v[18:25], v[212:219], v[118:121], v194, v194 op_sel_hi:[0,0,0]
	v_mfma_scale_f32_16x16x128_f8f6f4 v[114:117], v[26:33], v[212:219], v[114:117], v194, v194 op_sel_hi:[0,0,0]
	v_mfma_scale_f32_16x16x128_f8f6f4 v[102:105], v[18:25], v[220:227], v[102:105], v194, v194 op_sel_hi:[0,0,0]
	v_mfma_scale_f32_16x16x128_f8f6f4 v[98:101], v[26:33], v[220:227], v[98:101], v194, v194 op_sel_hi:[0,0,0]
	s_cbranch_vccz .Lwb_186l_2
	s_waitcnt vmcnt(8)
.Lwb_186l_2:
	s_setprio 0
	s_barrier
	s_add_u32 s36, s34, 0x2000
	s_addc_u32 s37, s35, 0
	s_add_i32 s0, s0, s40
	v_lshl_add_u64 v[228:229], s[36:37], 0, v[164:165]
	s_mov_b32 m0, s0
	ds_read_b128 v[196:199], v193 offset:49152
	ds_read_b128 v[200:203], v193 offset:50176
	ds_read_b128 v[204:207], v193 offset:51200
	ds_read_b128 v[208:211], v193 offset:52224
	ds_read_b128 v[212:215], v193 offset:53248
	ds_read_b128 v[216:219], v193 offset:54272
	ds_read_b128 v[220:223], v193 offset:55296
	ds_read_b128 v[224:227], v193 offset:56320
	global_load_lds_dwordx4 v[228:229], off
	s_add_i32 m0, s0, 0x2000
	s_add_u32 s34, s34, 0x42000
	v_lshl_add_u64 v[228:229], s[36:37], 0, v[168:169]
	s_addc_u32 s35, s35, 0
	s_add_i32 s0, s1, s40
	global_load_lds_dwordx4 v[228:229], off
	v_lshl_add_u64 v[228:229], s[34:35], 0, v[164:165]
	s_mov_b32 m0, s0
	v_lshl_add_u64 v[184:185], v[184:185], 0, s[12:13]
	global_load_lds_dwordx4 v[228:229], off
	v_lshl_add_u64 v[228:229], s[34:35], 0, v[168:169]
	s_add_i32 m0, s0, 0x2000
	s_nop 0
	global_load_lds_dwordx4 v[228:229], off
	s_mov_b32 m0, s44
	s_nop 0
	global_load_lds_dwordx4 v[184:185], off
	v_lshl_add_u64 v[184:185], v[186:187], 0, s[12:13]
	s_mov_b32 m0, s45
	s_nop 0
	global_load_lds_dwordx4 v[184:185], off
	s_and_b64 vcc, exec, s[14:15]
	s_cbranch_vccnz .Lwa_186l_3
	s_waitcnt vmcnt(8)
.Lwa_186l_3:
	s_waitcnt lgkmcnt(0)
	s_barrier
	s_setprio 1
	s_waitcnt lgkmcnt(0)
	v_mfma_scale_f32_16x16x128_f8f6f4 v[94:97], v[2:9], v[196:203], v[94:97], v194, v194 op_sel_hi:[0,0,0]
	v_mfma_scale_f32_16x16x128_f8f6f4 v[90:93], v[10:17], v[196:203], v[90:93], v194, v194 op_sel_hi:[0,0,0]
	v_mfma_scale_f32_16x16x128_f8f6f4 v[78:81], v[2:9], v[204:211], v[78:81], v194, v194 op_sel_hi:[0,0,0]
	v_mfma_scale_f32_16x16x128_f8f6f4 v[74:77], v[10:17], v[204:211], v[74:77], v194, v194 op_sel_hi:[0,0,0]
	v_mfma_scale_f32_16x16x128_f8f6f4 v[62:65], v[2:9], v[212:219], v[62:65], v194, v194 op_sel_hi:[0,0,0]
	v_mfma_scale_f32_16x16x128_f8f6f4 v[58:61], v[10:17], v[212:219], v[58:61], v194, v194 op_sel_hi:[0,0,0]
	v_mfma_scale_f32_16x16x128_f8f6f4 v[46:49], v[2:9], v[220:227], v[46:49], v194, v194 op_sel_hi:[0,0,0]
	v_mfma_scale_f32_16x16x128_f8f6f4 v[42:45], v[10:17], v[220:227], v[42:45], v194, v194 op_sel_hi:[0,0,0]
	s_setprio 0
	s_setprio 1
	v_mfma_scale_f32_16x16x128_f8f6f4 v[86:89], v[18:25], v[196:203], v[86:89], v194, v194 op_sel_hi:[0,0,0]
	v_mfma_scale_f32_16x16x128_f8f6f4 v[82:85], v[26:33], v[196:203], v[82:85], v194, v194 op_sel_hi:[0,0,0]
	v_mfma_scale_f32_16x16x128_f8f6f4 v[70:73], v[18:25], v[204:211], v[70:73], v194, v194 op_sel_hi:[0,0,0]
	v_mfma_scale_f32_16x16x128_f8f6f4 v[66:69], v[26:33], v[204:211], v[66:69], v194, v194 op_sel_hi:[0,0,0]
	v_mfma_scale_f32_16x16x128_f8f6f4 v[54:57], v[18:25], v[212:219], v[54:57], v194, v194 op_sel_hi:[0,0,0]
	v_mfma_scale_f32_16x16x128_f8f6f4 v[50:53], v[26:33], v[212:219], v[50:53], v194, v194 op_sel_hi:[0,0,0]
	v_mfma_scale_f32_16x16x128_f8f6f4 v[38:41], v[18:25], v[220:227], v[38:41], v194, v194 op_sel_hi:[0,0,0]
	v_mfma_scale_f32_16x16x128_f8f6f4 v[34:37], v[26:33], v[220:227], v[34:37], v194, v194 op_sel_hi:[0,0,0]
	s_cbranch_vccz .Lwb_186l_3
	s_waitcnt vmcnt(8)
.Lwb_186l_3:
	s_setprio 0
	s_barrier
	s_add_i32 s55, s55, 2
	s_add_u32 s53, s53, 0x4000
	s_addc_u32 s54, s54, 0
	s_add_u32 s30, s30, 0x100
	s_addc_u32 s31, s31, 0
	s_cmp_gt_u32 s55, 13
	s_cbranch_scc0 .LBB0_186
	s_and_b64 vcc, exec, s[14:15]
	s_cbranch_vccz .LBB0_189
	s_barrier
